# norm1 (layer 0) modulation parameter loads hoisted above the row reduction; GLA output epilogue gate/norm loads batched
# speedup vs baseline: 1.0408x; 1.0097x over previous
; __device__ __forceinline__ float row_rstd(const f32x4 (&v)[8]) {
;     float s = 0.f;
; #pragma unroll
;     for (int j = 0; j < 8; ++j) s += (v[j][0] * v[j][0] + v[j][1] * v[j][1]) + (v[j][2] * v[j][2] + v[j][3] * v[j][3]);
;     return rsqrtf(wave_sum(s) * (1.f / D) + NORM_EPS);
; }
; __device__ __forceinline__ void modulate(f32x4 (&v)[8], float rstd, const float* nw, const float* sh, const float* sc, int lane) {
; #pragma unroll
;     for (int j = 0; j < 8; ++j) { const f32x4 w = ((const f32x4*)nw)[lane + 64 * j], a = ((const f32x4*)sc)[lane + 64 * j], b = ((const f32x4*)sh)[lane + 64 * j];
;         v[j] = v[j] * rstd * w * (a + 1.f) + b; }
; }
; __device__ __forceinline__ void ph_norm1(KP Pk, Frame& F, int l) {
;     ...
;     for (int row = rfirst; row < rend; row += rstep) {
;         const int r = modrow_of(row); f32x4 v[8];
;         if (l == 0) load_row(row < TL ? Pk->in[I_X] + (size_t)row * D : Pk->in[I_CTX] + (size_t)(row - TL) * D, F.lane, v);
;         else { load_row_bf16(X + (size_t)row * D, F.lane, v);
;             add_y2(Y2 + (size_t)row * D, Y2 + ((size_t)TT + row) * D, (const float*)(ws + WS_MOD) + (size_t)r * 12288 + 5 * D, F.lane, v);
;             if (row < TL) store_row_bf16(X + (size_t)row * D, F.lane, v); }
;         const float rstd = row_rstd(v);
;         modulate(v, rstd, Pk->in[I_N1W] + l * D, mod + (size_t)r * 12288, mod + (size_t)r * 12288 + D, F.lane);
;         if (WIN_F8_L(l)) store_row_f8(ws + WS_H + (size_t)row * D, F.lane, v); else store_row_bf16(H + (size_t)row * D, F.lane, v);
.LBB0_190:
	s_waitcnt vmcnt(7)
	v_pk_mul_f32 v[64:65], v[30:31], v[30:31]
	s_waitcnt vmcnt(6)
	v_pk_mul_f32 v[66:67], v[26:27], v[26:27]
	v_pk_mul_f32 v[60:61], v[32:33], v[32:33]
	v_pk_mul_f32 v[62:63], v[28:29], v[28:29]
	v_mov_b32_e32 v74, v64
	v_mov_b32_e32 v75, v66
	v_mov_b32_e32 v66, v65
	s_waitcnt vmcnt(5)
	v_pk_mul_f32 v[56:57], v[24:25], v[24:25]
	v_pk_mul_f32 v[58:59], v[22:23], v[22:23]
	v_pk_add_f32 v[64:65], v[74:75], v[66:67]
	v_mov_b32_e32 v66, v60
	v_mov_b32_e32 v67, v62
	v_mov_b32_e32 v62, v61
	v_pk_add_f32 v[60:61], v[66:67], v[62:63]
	v_pk_mov_b32 v[62:63], v[58:59], v[56:57] op_sel:[1,0]
	v_mov_b32_e32 v59, v57
	v_pk_add_f32 v[56:57], v[62:63], v[58:59]
	v_pk_add_f32 v[60:61], v[64:65], v[60:61]
	v_pk_add_f32 v[56:57], v[56:57], v[56:57] op_sel_hi:[0,1]
	s_waitcnt vmcnt(4)
	v_mul_f32_e32 v56, v18, v18
	v_pk_fma_f32 v[58:59], v[18:19], v[18:19], v[56:57] op_sel_hi:[1,1,0]
	v_mul_f32_e32 v56, v20, v20
	v_pk_add_f32 v[60:61], v[60:61], v[60:61] op_sel_hi:[0,1]
	v_pk_fma_f32 v[62:63], v[20:21], v[20:21], v[56:57] op_sel_hi:[1,1,0]
	s_waitcnt vmcnt(3)
	v_mul_f32_e32 v58, v14, v14
	v_mul_f32_e32 v62, v15, v15
	v_mul_f32_e32 v56, v16, v16
	v_mul_f32_e32 v60, v17, v17
	s_waitcnt vmcnt(2)
	v_pk_mul_f32 v[52:53], v[12:13], v[12:13]
	v_pk_mul_f32 v[54:55], v[10:11], v[10:11]
	v_pk_add_f32 v[58:59], v[58:59], v[62:63]
	v_pk_add_f32 v[56:57], v[56:57], v[60:61]
	s_add_u32 s50, s7, s37
	v_pk_add_f32 v[56:57], v[58:59], v[56:57]
	v_pk_mov_b32 v[58:59], v[54:55], v[52:53] op_sel:[1,0]
	v_mov_b32_e32 v55, v53
	v_pk_add_f32 v[52:53], v[58:59], v[54:55]
	v_pk_add_f32 v[56:57], v[56:57], v[56:57] op_sel_hi:[0,1]
	v_pk_add_f32 v[52:53], v[52:53], v[52:53] op_sel_hi:[0,1]
	s_waitcnt vmcnt(1)
	v_mul_f32_e32 v52, v6, v6
	v_pk_fma_f32 v[54:55], v[6:7], v[6:7], v[52:53] op_sel_hi:[1,1,0]
	v_mul_f32_e32 v52, v8, v8
	v_pk_fma_f32 v[58:59], v[8:9], v[8:9], v[52:53] op_sel_hi:[1,1,0]
	s_waitcnt vmcnt(0)
	v_mul_f32_e32 v54, v2, v2
	v_mul_f32_e32 v58, v3, v3
	v_mul_f32_e32 v52, v4, v4
	v_mul_f32_e32 v56, v5, v5
	v_pk_add_f32 v[54:55], v[54:55], v[58:59]
	v_pk_add_f32 v[52:53], v[52:53], v[56:57]
	s_addc_u32 s51, s18, s19
	v_pk_add_f32 v[52:53], v[54:55], v[52:53]
	v_lshl_add_u64 v[54:55], v[34:35], 4, s[50:51]
	v_add_f32_e32 v52, v52, v53
	ds_bpermute_b32 v53, v1, v52
	s_movk_i32 s17, 0x3000
	s_mov_b64 s[50:51], 0x2000
	v_lshl_add_u64 v[64:65], v[54:55], 0, s[50:51]
	v_add_co_u32_e32 v66, vcc, s17, v54
	s_nop 1
	v_addc_co_u32_e32 v67, vcc, 0, v55, vcc
	v_add_co_u32_e32 v78, vcc, s1, v54
	s_nop 1
	v_addc_co_u32_e32 v79, vcc, 0, v55, vcc
	global_load_dwordx4 v[120:123], v[36:37], off
	global_load_dwordx4 v[124:127], v[66:67], off offset:-4096
	global_load_dwordx4 v[128:131], v[54:55], off
	global_load_dwordx4 v[132:135], v[36:37], off offset:1024
	global_load_dwordx4 v[136:139], v[64:65], off offset:1024
	global_load_dwordx4 v[140:143], v[54:55], off offset:1024
	global_load_dwordx4 v[144:147], v[36:37], off offset:2048
	global_load_dwordx4 v[148:151], v[64:65], off offset:2048
	global_load_dwordx4 v[152:155], v[54:55], off offset:2048
	global_load_dwordx4 v[156:159], v[36:37], off offset:3072
	global_load_dwordx4 v[160:163], v[64:65], off offset:3072
	global_load_dwordx4 v[164:167], v[54:55], off offset:3072
	global_load_dwordx4 v[168:171], v[38:39], off
	global_load_dwordx4 v[172:175], v[66:67], off
	global_load_dwordx4 v[176:179], v[78:79], off
	global_load_dwordx4 v[180:183], v[40:41], off
	global_load_dwordx4 v[184:187], v[66:67], off offset:1024
	global_load_dwordx4 v[188:191], v[78:79], off offset:1024
	global_load_dwordx4 v[196:199], v[42:43], off
	global_load_dwordx4 v[200:203], v[66:67], off offset:2048
	global_load_dwordx4 v[204:207], v[78:79], off offset:2048
	global_load_dwordx4 v[208:211], v[44:45], off
	global_load_dwordx4 v[212:215], v[66:67], off offset:3072
	global_load_dwordx4 v[216:219], v[78:79], off offset:3072
	s_waitcnt lgkmcnt(0)
	v_add_f32_e32 v52, v52, v53
	ds_bpermute_b32 v53, v68, v52
	s_add_i32 s16, s16, s26
	s_add_u32 s38, s38, s26
	s_addc_u32 s39, s39, s27
	s_add_u32 s40, s40, s42
	s_waitcnt lgkmcnt(0)
	v_add_f32_e32 v52, v52, v53
	ds_bpermute_b32 v53, v69, v52
	s_addc_u32 s41, s41, s43
	s_add_u32 s44, s44, s46
	s_addc_u32 s45, s45, s47
	v_lshl_add_u64 v[50:51], v[50:51], 0, s[48:49]
	s_waitcnt lgkmcnt(0)
	v_add_f32_e32 v52, v52, v53
	ds_bpermute_b32 v53, v70, v52
	s_cmp_lt_i32 s16, s4
	s_waitcnt lgkmcnt(0)
	v_add_f32_e32 v52, v52, v53
	ds_bpermute_b32 v53, v71, v52
	s_waitcnt lgkmcnt(0)
	v_add_f32_e32 v52, v52, v53
	ds_bpermute_b32 v53, v72, v52
	s_waitcnt lgkmcnt(0)
	v_add_f32_e32 v52, v52, v53
	v_fmamk_f32 v52, v52, 0x3a000000, v194
	v_cmp_gt_f32_e32 vcc, s66, v52
	v_mul_f32_e32 v53, 0x4b800000, v52
	s_nop 0
	v_cndmask_b32_e32 v52, v52, v53, vcc
	v_rsq_f32_e32 v52, v52
	s_nop 0
	v_mul_f32_e32 v53, 0x45800000, v52
	v_cndmask_b32_e32 v52, v52, v53, vcc
	v_add_co_u32_e32 v66, vcc, s17, v54
	v_pk_mul_f32 v[32:33], v[32:33], v[52:53] op_sel_hi:[1,0]
	s_nop 0
	v_addc_co_u32_e32 v67, vcc, 0, v55, vcc
	v_pk_mul_f32 v[30:31], v[30:31], v[52:53] op_sel_hi:[1,0]
	v_pk_mul_f32 v[28:29], v[28:29], v[52:53] op_sel_hi:[1,0]
	v_pk_mul_f32 v[26:27], v[26:27], v[52:53] op_sel_hi:[1,0]
	v_pk_mul_f32 v[24:25], v[24:25], v[52:53] op_sel_hi:[1,0]
	v_pk_mul_f32 v[22:23], v[22:23], v[52:53] op_sel_hi:[1,0]
	v_pk_mul_f32 v[20:21], v[20:21], v[52:53] op_sel_hi:[1,0]
	v_pk_mul_f32 v[18:19], v[18:19], v[52:53] op_sel_hi:[1,0]
	v_add_co_u32_e32 v78, vcc, s1, v54
	v_pk_mul_f32 v[16:17], v[16:17], v[52:53] op_sel_hi:[1,0]
	s_nop 0
	v_addc_co_u32_e32 v79, vcc, 0, v55, vcc
	v_pk_mul_f32 v[14:15], v[14:15], v[52:53] op_sel_hi:[1,0]
	v_pk_mul_f32 v[12:13], v[12:13], v[52:53] op_sel_hi:[1,0]
	v_pk_mul_f32 v[10:11], v[10:11], v[52:53] op_sel_hi:[1,0]
	v_pk_mul_f32 v[8:9], v[8:9], v[52:53] op_sel_hi:[1,0]
	v_pk_mul_f32 v[6:7], v[6:7], v[52:53] op_sel_hi:[1,0]
	v_pk_mul_f32 v[2:3], v[2:3], v[52:53] op_sel_hi:[1,0]
	v_pk_mul_f32 v[4:5], v[4:5], v[52:53] op_sel_hi:[1,0]
	s_waitcnt vmcnt(0)
; __device__ __forceinline__ unsigned pk2(float lo, float hi) { return f2bf(lo) | (f2bf(hi) << 16); }
; __device__ __forceinline__ unsigned pk2q(float lo, float hi) { return f2bf(q8(lo)) | (f2bf(q8(hi)) << 16); }
; __device__ __forceinline__ void modulate(f32x4 (&v)[8], float rstd, const float* nw, const float* sh, const float* sc, int lane) {
; #pragma unroll
;     for (int j = 0; j < 8; ++j) { const f32x4 w = ((const f32x4*)nw)[lane + 64 * j], a = ((const f32x4*)sc)[lane + 64 * j], b = ((const f32x4*)sh)[lane + 64 * j];
;         v[j] = v[j] * rstd * w * (a + 1.f) + b; }
; }
; __device__ __forceinline__ void store_row_bf16(bf16_t* o, int lane, const f32x4 (&v)[8], bool q = false) {
; #pragma unroll
;     for (int j = 0; j < 8; ++j) { u32x2 w; if (q) { w.x = pk2q(v[j][0], v[j][1]); w.y = pk2q(v[j][2], v[j][3]); } else { w.x = pk2(v[j][0], v[j][1]); w.y = pk2(v[j][2], v[j][3]); } ((u32x2*)o)[lane + 64 * j] = w; }
; }
; __device__ __forceinline__ void store_row_f8(unsigned char* o, int lane, const f32x4 (&v)[8]) {
; #pragma unroll
;     for (int j = 0; j < 8; ++j) ((unsigned*)o)[lane + 64 * j] = pk4_f8(v[j][0], v[j][1], v[j][2], v[j][3]);
; }
	v_pk_mul_f32 v[56:57], v[120:121], v[30:31]
	v_pk_mul_f32 v[30:31], v[122:123], v[32:33]
	v_pk_add_f32 v[32:33], v[126:127], 1.0 op_sel_hi:[1,0]
	v_pk_add_f32 v[58:59], v[124:125], 1.0 op_sel_hi:[1,0]
	v_pk_fma_f32 v[30:31], v[32:33], v[30:31], v[130:131]
	v_pk_fma_f32 v[32:33], v[58:59], v[56:57], v[128:129]
	v_pk_mul_f32 v[56:57], v[132:133], v[26:27]
	v_pk_mul_f32 v[26:27], v[134:135], v[28:29]
	v_pk_add_f32 v[28:29], v[138:139], 1.0 op_sel_hi:[1,0]
	v_pk_add_f32 v[58:59], v[136:137], 1.0 op_sel_hi:[1,0]
	v_pk_fma_f32 v[26:27], v[28:29], v[26:27], v[142:143]
	v_pk_fma_f32 v[28:29], v[58:59], v[56:57], v[140:141]
	v_pk_mul_f32 v[56:57], v[144:145], v[22:23]
	v_pk_mul_f32 v[22:23], v[146:147], v[24:25]
	v_pk_add_f32 v[24:25], v[150:151], 1.0 op_sel_hi:[1,0]
	v_pk_add_f32 v[58:59], v[148:149], 1.0 op_sel_hi:[1,0]
	v_pk_fma_f32 v[22:23], v[24:25], v[22:23], v[154:155]
	v_pk_fma_f32 v[24:25], v[58:59], v[56:57], v[152:153]
	v_pk_mul_f32 v[56:57], v[156:157], v[18:19]
	v_pk_mul_f32 v[18:19], v[158:159], v[20:21]
	v_pk_add_f32 v[20:21], v[162:163], 1.0 op_sel_hi:[1,0]
	v_pk_add_f32 v[58:59], v[160:161], 1.0 op_sel_hi:[1,0]
	v_pk_fma_f32 v[18:19], v[20:21], v[18:19], v[166:167]
	v_pk_fma_f32 v[20:21], v[58:59], v[56:57], v[164:165]
	v_pk_mul_f32 v[14:15], v[168:169], v[14:15]
	v_pk_mul_f32 v[16:17], v[170:171], v[16:17]
	v_pk_add_f32 v[54:55], v[174:175], 1.0 op_sel_hi:[1,0]
	v_pk_add_f32 v[56:57], v[172:173], 1.0 op_sel_hi:[1,0]
	v_pk_fma_f32 v[54:55], v[54:55], v[16:17], v[178:179]
	v_pk_fma_f32 v[56:57], v[56:57], v[14:15], v[176:177]
	v_pk_mul_f32 v[10:11], v[180:181], v[10:11]
	v_pk_mul_f32 v[12:13], v[182:183], v[12:13]
	v_pk_add_f32 v[14:15], v[186:187], 1.0 op_sel_hi:[1,0]
	v_pk_add_f32 v[16:17], v[184:185], 1.0 op_sel_hi:[1,0]
	v_pk_fma_f32 v[58:59], v[14:15], v[12:13], v[190:191]
	v_pk_fma_f32 v[60:61], v[16:17], v[10:11], v[188:189]
	v_pk_mul_f32 v[6:7], v[196:197], v[6:7]
	v_pk_mul_f32 v[8:9], v[198:199], v[8:9]
	v_pk_add_f32 v[10:11], v[202:203], 1.0 op_sel_hi:[1,0]
	v_pk_add_f32 v[12:13], v[200:201], 1.0 op_sel_hi:[1,0]
	v_pk_fma_f32 v[62:63], v[10:11], v[8:9], v[206:207]
	v_pk_fma_f32 v[64:65], v[12:13], v[6:7], v[204:205]
	v_pk_mul_f32 v[2:3], v[2:3], v[208:209]
	v_pk_add_f32 v[6:7], v[212:213], 1.0 op_sel_hi:[1,0]
	v_mov_b32_e32 v10, v0
	v_pk_fma_f32 v[2:3], v[2:3], v[6:7], v[216:217]
	v_med3_f32 v6, v32, s83, v238
	v_med3_f32 v7, v33, s83, v238
	v_cvt_pk_fp8_f32 v10, v6, v7
	v_pk_mul_f32 v[4:5], v[4:5], v[210:211]
	v_pk_add_f32 v[8:9], v[214:215], 1.0 op_sel_hi:[1,0]
	v_mov_b32_e32 v12, v0
	v_pk_fma_f32 v[4:5], v[4:5], v[8:9], v[218:219]
	v_med3_f32 v8, v30, s83, v238
	v_med3_f32 v9, v31, s83, v238
	v_cvt_pk_fp8_f32 v10, v8, v9 op_sel:[0,0,1]
	v_med3_f32 v8, v28, s83, v238
	v_med3_f32 v9, v29, s83, v238
	v_cvt_pk_fp8_f32 v12, v8, v9
	v_lshl_add_u64 v[6:7], v[48:49], 0, s[34:35]
	global_store_dword v[6:7], v10, off
	v_med3_f32 v10, v26, s83, v238
	v_med3_f32 v11, v27, s83, v238
	v_cvt_pk_fp8_f32 v12, v10, v11 op_sel:[0,0,1]
	v_med3_f32 v8, v24, s83, v238
	v_med3_f32 v9, v25, s83, v238
	v_med3_f32 v10, v22, s83, v238
	global_store_dword v[6:7], v12, off offset:256
	v_mov_b32_e32 v12, v0
	v_cvt_pk_fp8_f32 v12, v8, v9
	v_med3_f32 v11, v23, s83, v238
	v_med3_f32 v8, v20, s83, v238
	v_med3_f32 v9, v21, s83, v238
	v_cvt_pk_fp8_f32 v12, v10, v11 op_sel:[0,0,1]
	v_med3_f32 v10, v18, s83, v238
	v_med3_f32 v11, v19, s83, v238
	v_med3_f32 v2, v2, s83, v238
	global_store_dword v[6:7], v12, off offset:512
	v_mov_b32_e32 v12, v0
	v_cvt_pk_fp8_f32 v12, v8, v9
	v_med3_f32 v8, v56, s83, v238
	v_med3_f32 v9, v57, s83, v238
	v_med3_f32 v3, v3, s83, v238
	v_cvt_pk_fp8_f32 v12, v10, v11 op_sel:[0,0,1]
	v_med3_f32 v10, v54, s83, v238
	v_med3_f32 v11, v55, s83, v238
	v_med3_f32 v4, v4, s83, v238
	global_store_dword v[6:7], v12, off offset:768
	v_mov_b32_e32 v12, v0
	v_cvt_pk_fp8_f32 v12, v8, v9
	v_med3_f32 v8, v60, s83, v238
	v_med3_f32 v9, v61, s83, v238
	v_med3_f32 v5, v5, s83, v238
	v_cvt_pk_fp8_f32 v12, v10, v11 op_sel:[0,0,1]
	v_med3_f32 v10, v58, s83, v238
	v_med3_f32 v11, v59, s83, v238
	global_store_dword v[6:7], v12, off offset:1024
	v_mov_b32_e32 v12, v0
	v_cvt_pk_fp8_f32 v12, v8, v9
	v_med3_f32 v8, v64, s83, v238
	v_med3_f32 v9, v65, s83, v238
	v_cvt_pk_fp8_f32 v12, v10, v11 op_sel:[0,0,1]
	v_med3_f32 v10, v62, s83, v238
	v_med3_f32 v11, v63, s83, v238
	global_store_dword v[6:7], v12, off offset:1280
	v_mov_b32_e32 v12, v0
	v_cvt_pk_fp8_f32 v12, v8, v9
	v_mov_b32_e32 v8, v0
	v_cvt_pk_fp8_f32 v8, v2, v3
	v_cvt_pk_fp8_f32 v12, v10, v11 op_sel:[0,0,1]
	v_cvt_pk_fp8_f32 v8, v4, v5 op_sel:[0,0,1]
	global_store_dword v[6:7], v12, off offset:1536
	global_store_dword v[6:7], v8, off offset:1792
	s_cbranch_scc0 .LBB0_200

; __device__ __forceinline__ float silu_f(float x) { return x / (1.f + __expf(-x)); }
; __device__ __forceinline__ void gla_pass_b(KP Pk, Frame& F, int l, int b, int h, int c, LAS unsigned char* wl) {
;     ...
;                 for (int nb = 0; nb < 4; ++nb) { o[nb][0] += bflo(t[nb].x); o[nb][1] += bfhi(t[nb].x); o[nb][2] += bflo(t[nb].y); o[nb][3] += bfhi(t[nb].y); ss += (o[nb][0] * o[nb][0] + o[nb][1] * o[nb][1]) + (o[nb][2] * o[nb][2] + o[nb][3] * o[nb][3]); }
;                 ss += __shfl_xor(ss, 16); ss += __shfl_xor(ss, 32);
;                 const float rstd = rsqrtf(ss * (1.f / 64.f) + NORM_EPS); const int row = keyrow(b, 64 * c + 16 * sb + r16);
; #pragma unroll
;                 for (int nb = 0; nb < 4; ++nb) { const int dv0 = 16 * nb + 4 * kg; const u32x2 gg = *(const u32x2*)(U + (size_t)row * NU + UC_GG + h * 64 + dv0); const f32x4 nw = *(const f32x4*)(Pk->in[I_GNW] + l * 64 + dv0);
;                     const float y0 = o[nb][0] * rstd * nw[0] * silu_f(bflo(gg.x)), y1 = o[nb][1] * rstd * nw[1] * silu_f(bfhi(gg.x)), y2 = o[nb][2] * rstd * nw[2] * silu_f(bflo(gg.y)), y3 = o[nb][3] * rstd * nw[3] * silu_f(bfhi(gg.y));
;                     if (WOUT_F8) *(unsigned*)(MIX + ((size_t)row * D + h * 64 + dv0)) = pk4_f8(y0, y1, y2, y3);
.LBB0_670:
	v_lshlrev_b32_e32 v59, 16, v52
	v_and_b32_e32 v52, 0xffff0000, v52
	v_add_f32_e32 v169, v35, v52
	v_lshlrev_b32_e32 v52, 16, v53
	v_add_f32_e32 v167, v36, v52
	v_and_b32_e32 v52, 0xffff0000, v53
	v_add_f32_e32 v164, v37, v52
	v_lshlrev_b32_e32 v52, 16, v50
	v_and_b32_e32 v50, 0xffff0000, v50
	v_add_f32_e32 v162, v39, v50
	v_lshlrev_b32_e32 v50, 16, v51
	v_or_b32_e32 v1, s5, v1
	v_add_f32_e32 v163, v38, v52
	v_add_f32_e32 v161, v40, v50
	v_and_b32_e32 v52, 0xffff0000, v51
	v_add_u32_e32 v156, s37, v1
	v_mov_b64_e32 v[50:51], s[50:51]
	v_mad_i64_i32 v[50:51], s[34:35], v156, s30, v[50:51]
	s_mov_b32 s63, s61
	v_add_f32_e32 v170, v34, v59
	v_lshl_add_u64 v[50:51], v[50:51], 0, s[62:63]
	v_ashrrev_i32_e32 v59, 31, v58
	v_lshl_add_u64 v[146:147], v[58:59], 1, v[50:51]
	s_mov_b32 s5, 0x2ae00000
	v_add_co_u32_e32 v50, vcc, s5, v146
	s_load_dwordx2 s[34:35], s[48:49], 0x60
	s_nop 0
	v_addc_co_u32_e32 v51, vcc, 0, v147, vcc
	v_lshlrev_b32_e32 v50, 16, v56
	s_waitcnt lgkmcnt(0)
	s_add_u32 s34, s34, s52
	s_addc_u32 s35, s35, s53
	v_lshl_add_u64 v[142:143], v[58:59], 2, s[34:35]
	v_add_f32_e32 v168, v41, v52
	v_add_f32_e32 v166, v42, v50
	v_add_co_u32_e32 v224, vcc, 0x2ae00800, v146
	s_nop 1
	v_addc_co_u32_e32 v225, vcc, 0, v147, vcc
	global_load_dwordx2 v[250:251], v[224:225], off
	global_load_dwordx4 v[208:211], v[142:143], off
	global_load_dwordx2 v[222:223], v[224:225], off offset:32
	global_load_dwordx4 v[212:215], v[142:143], off offset:64
	global_load_dwordx2 v[242:243], v[224:225], off offset:64
	global_load_dwordx4 v[216:219], v[142:143], off offset:128
	global_load_dwordx4 v[244:247], v[142:143], off offset:192
	global_load_dwordx2 v[248:249], v[224:225], off offset:96
	v_and_b32_e32 v56, 0xffff0000, v56
	v_add_f32_e32 v165, v43, v56
	v_lshlrev_b32_e32 v56, 16, v57
	v_and_b32_e32 v57, 0xffff0000, v57
	v_pk_add_f32 v[144:145], v[44:45], v[56:57]
	v_mul_f32_e32 v173, v163, v163
	v_mul_f32_e32 v56, v144, v144
	v_pk_fma_f32 v[184:185], v[144:145], v[144:145], v[56:57] op_sel_hi:[1,1,0]
	v_lshlrev_b32_e32 v56, 16, v54
	v_mul_f32_e32 v179, v162, v162
	v_mul_f32_e32 v1, v168, v168
	v_add_f32_e32 v60, v46, v56
	v_lshlrev_b32_e32 v178, 16, v55
	v_mov_b32_e32 v172, v48
	v_mul_f32_e32 v155, v170, v170
	v_mul_f32_e32 v151, v169, v169
	v_mul_f32_e32 v157, v164, v164
	v_mul_f32_e32 v181, v161, v161
	v_mul_f32_e32 v61, v166, v166
	v_mul_f32_e32 v183, v165, v165
	v_and_b32_e32 v54, 0xffff0000, v54
	v_and_b32_e32 v150, 0xffff0000, v55
	v_pk_add_f32 v[56:57], v[172:173], v[178:179]
	v_mov_b32_e32 v180, v48
	v_mov_b32_e32 v179, v1
	v_mov_b32_e32 v154, v49
	v_mov_b32_e32 v182, v60
	v_mul_f32_e32 v153, v167, v167
	v_add_f32_e32 v160, v47, v54
	v_pk_add_f32 v[172:173], v[180:181], v[178:179]
	v_pk_add_f32 v[54:55], v[154:155], v[150:151]
	v_mov_b32_e32 v152, v49
	v_mov_b32_e32 v151, v157
	v_pk_add_f32 v[154:155], v[60:61], v[182:183]
	v_pk_add_f32 v[150:151], v[152:153], v[150:151]
	v_mov_b32_e32 v153, v155
	v_pk_mul_f32 v[154:155], v[56:57], v[172:173]
	v_pk_add_f32 v[172:173], v[56:57], v[172:173]
	v_mul_f32_e32 v184, v160, v160
	v_mov_b32_e32 v155, v173
	v_pk_mul_f32 v[172:173], v[54:55], v[150:151]
	v_pk_add_f32 v[150:151], v[54:55], v[150:151]
	v_mul_f32_e32 v152, v60, v60
	v_mov_b32_e32 v173, v151
	v_pk_add_f32 v[152:153], v[152:153], v[184:185]
	v_pk_add_f32 v[150:151], v[154:155], v[172:173]
	v_cmp_lt_i32_e32 vcc, v232, v234
	v_pk_add_f32 v[150:151], v[152:153], v[150:151]
	v_ashrrev_i32_e32 v157, 31, v156
	v_cndmask_b32_e32 v55, v231, v232, vcc
	v_add_f32_e32 v1, v150, v151
	v_lshlrev_b32_e32 v55, 2, v55
	ds_bpermute_b32 v55, v55, v1
	v_cmp_lt_i32_e32 vcc, v235, v234
	v_lshlrev_b64 v[150:151], 11, v[156:157]
	v_lshl_add_u64 v[150:151], s[42:43], 0, v[150:151]
	v_lshl_add_u64 v[58:59], v[150:151], 0, v[58:59]
	s_waitcnt lgkmcnt(0)
	v_add_f32_e32 v1, v1, v55
	v_cndmask_b32_e32 v55, v231, v235, vcc
	v_lshlrev_b32_e32 v55, 2, v55
	ds_bpermute_b32 v55, v55, v1
	s_waitcnt lgkmcnt(0)
	v_add_f32_e32 v1, v1, v55
	v_fmamk_f32 v1, v1, 0x3c800000, v194
	v_mul_f32_e32 v55, 0x4b800000, v1
	v_cmp_gt_f32_e32 vcc, s66, v1
	s_waitcnt vmcnt(0)
	v_lshlrev_b32_e32 v57, 16, v250
	v_cndmask_b32_e32 v1, v1, v55, vcc
	v_rsq_f32_e32 v1, v1
	v_mul_f32_e32 v61, 0xbfb8aa3b, v57
	v_exp_f32_e32 v61, v61
	v_and_b32_e32 v148, 0xffff0000, v250
	v_mul_f32_e32 v55, 0x45800000, v1
	v_cndmask_b32_e32 v1, v1, v55, vcc
	v_add_f32_e32 v55, 1.0, v61
	v_div_scale_f32 v61, s[34:35], v55, v55, v57
	v_rcp_f32_e32 v152, v61
	v_mul_f32_e32 v153, v170, v1
	v_mul_f32_e32 v50, v208, v153
	v_mul_f32_e32 v151, v163, v1
	v_fma_f32 v153, -v61, v152, 1.0
	v_fmac_f32_e32 v152, v153, v152
	v_div_scale_f32 v153, vcc, v57, v55, v57
	v_mul_f32_e32 v154, v153, v152
	v_fma_f32 v155, -v61, v154, v153
	v_fmac_f32_e32 v154, v155, v152
	v_fma_f32 v61, -v61, v154, v153
	v_mul_f32_e32 v153, 0xbfb8aa3b, v148
	v_exp_f32_e32 v153, v153
	v_div_fmas_f32 v61, v61, v152, v154
	v_div_fixup_f32 v55, v61, v55, v57
	v_mul_f32_e32 v50, v55, v50
	v_add_f32_e32 v57, 1.0, v153
	v_div_scale_f32 v61, s[34:35], v57, v57, v148
	v_rcp_f32_e32 v152, v61
	v_mul_f32_e32 v55, v169, v1
	v_mul_f32_e32 v51, v209, v55
	v_med3_f32 v50, v50, s83, v238
	v_fma_f32 v55, -v61, v152, 1.0
	v_fmac_f32_e32 v152, v55, v152
	v_div_scale_f32 v55, vcc, v148, v57, v148
	v_mul_f32_e32 v153, v55, v152
	v_fma_f32 v154, -v61, v153, v55
	v_fmac_f32_e32 v153, v154, v152
	v_fma_f32 v55, -v61, v153, v55
	v_lshlrev_b32_e32 v61, 16, v251
	v_mul_f32_e32 v154, 0xbfb8aa3b, v61
	v_exp_f32_e32 v154, v154
	v_div_fmas_f32 v55, v55, v152, v153
	v_div_fixup_f32 v55, v55, v57, v148
	v_mul_f32_e32 v51, v55, v51
	v_add_f32_e32 v57, 1.0, v154
	v_div_scale_f32 v148, s[34:35], v57, v57, v61
; __device__ __forceinline__ float silu_f(float x) { return x / (1.f + __expf(-x)); }
; __device__ __forceinline__ unsigned pk4_f8(float a, float b, float c, float d) {
;     a = fminf(fmaxf(a, -448.f), 448.f); b = fminf(fmaxf(b, -448.f), 448.f); c = fminf(fmaxf(c, -448.f), 448.f); d = fminf(fmaxf(d, -448.f), 448.f);
;     int r = 0; r = __builtin_amdgcn_cvt_pk_fp8_f32(a, b, r, false); r = __builtin_amdgcn_cvt_pk_fp8_f32(c, d, r, true); return (unsigned)r; }
; __device__ __forceinline__ void gla_pass_b(KP Pk, Frame& F, int l, int b, int h, int c, LAS unsigned char* wl) {
;     ...
;                 for (int nb = 0; nb < 4; ++nb) { const int dv0 = 16 * nb + 4 * kg; const u32x2 gg = *(const u32x2*)(U + (size_t)row * NU + UC_GG + h * 64 + dv0); const f32x4 nw = *(const f32x4*)(Pk->in[I_GNW] + l * 64 + dv0);
;                     const float y0 = o[nb][0] * rstd * nw[0] * silu_f(bflo(gg.x)), y1 = o[nb][1] * rstd * nw[1] * silu_f(bfhi(gg.x)), y2 = o[nb][2] * rstd * nw[2] * silu_f(bflo(gg.y)), y3 = o[nb][3] * rstd * nw[3] * silu_f(bfhi(gg.y));
;                     if (WOUT_F8) *(unsigned*)(MIX + ((size_t)row * D + h * 64 + dv0)) = pk4_f8(y0, y1, y2, y3);
	v_rcp_f32_e32 v152, v148
	v_mul_f32_e32 v55, v167, v1
	v_mul_f32_e32 v52, v210, v55
	v_med3_f32 v51, v51, s83, v238
	v_fma_f32 v55, -v148, v152, 1.0
	v_fmac_f32_e32 v152, v55, v152
	v_div_scale_f32 v55, vcc, v61, v57, v61
	v_mul_f32_e32 v153, v55, v152
	v_fma_f32 v154, -v148, v153, v55
	v_fmac_f32_e32 v153, v154, v152
	v_fma_f32 v55, -v148, v153, v55
	v_and_b32_e32 v148, 0xffff0000, v251
	v_mul_f32_e32 v149, 0xbfb8aa3b, v148
	v_exp_f32_e32 v149, v149
	v_div_fmas_f32 v55, v55, v152, v153
	v_div_fixup_f32 v55, v55, v57, v61
	v_mul_f32_e32 v52, v55, v52
	v_add_f32_e32 v57, 1.0, v149
	v_div_scale_f32 v61, s[34:35], v57, v57, v148
	v_rcp_f32_e32 v149, v61
	v_mul_f32_e32 v55, v164, v1
	v_mul_f32_e32 v53, v211, v55
	s_mov_b64 s[34:35], 0x2ae00800
	v_fma_f32 v55, -v61, v149, 1.0
	v_fmac_f32_e32 v149, v55, v149
	v_div_scale_f32 v55, vcc, v148, v57, v148
	v_mul_f32_e32 v152, v55, v149
	v_fma_f32 v153, -v61, v152, v55
	v_fmac_f32_e32 v152, v153, v149
	v_fma_f32 v55, -v61, v152, v55
	v_div_fmas_f32 v55, v55, v149, v152
	v_div_fixup_f32 v55, v55, v57, v148
	v_mov_b32_e32 v57, v0
	v_cvt_pk_fp8_f32 v57, v50, v51
	v_mul_f32_e32 v50, v55, v53
	v_med3_f32 v51, v52, s83, v238
	v_med3_f32 v50, v50, s83, v238
	v_cvt_pk_fp8_f32 v57, v51, v50 op_sel:[0,0,1]
	v_lshl_add_u64 v[146:147], v[146:147], 0, s[34:35]
	v_mul_f32_e32 v56, v56, v1
	global_store_dword v[58:59], v57, off
	v_lshlrev_b32_e32 v55, 16, v222
	v_mul_f32_e32 v57, 0xbfb8aa3b, v55
	v_exp_f32_e32 v57, v57
	v_mul_f32_e32 v50, v212, v151
	v_and_b32_e32 v148, 0xffff0000, v222
	v_add_f32_e32 v57, 1.0, v57
	v_div_scale_f32 v61, s[34:35], v57, v57, v55
	v_rcp_f32_e32 v150, v61
	s_nop 0
	v_fma_f32 v151, -v61, v150, 1.0
	v_fmac_f32_e32 v150, v151, v150
	v_div_scale_f32 v151, vcc, v55, v57, v55
	v_mul_f32_e32 v152, v151, v150
	v_fma_f32 v153, -v61, v152, v151
	v_fmac_f32_e32 v152, v153, v150
	v_fma_f32 v61, -v61, v152, v151
	v_mul_f32_e32 v151, 0xbfb8aa3b, v148
	v_exp_f32_e32 v151, v151
	v_div_fmas_f32 v61, v61, v150, v152
	v_div_fixup_f32 v55, v61, v57, v55
	v_mul_f32_e32 v50, v55, v50
	v_add_f32_e32 v57, 1.0, v151
	v_div_scale_f32 v61, s[34:35], v57, v57, v148
	v_rcp_f32_e32 v150, v61
	v_mul_f32_e32 v55, v162, v1
	v_mul_f32_e32 v51, v213, v55
	v_med3_f32 v50, v50, s83, v238
	v_fma_f32 v55, -v61, v150, 1.0
	v_fmac_f32_e32 v150, v55, v150
	v_div_scale_f32 v55, vcc, v148, v57, v148
	v_mul_f32_e32 v151, v55, v150
	v_fma_f32 v152, -v61, v151, v55
	v_fmac_f32_e32 v151, v152, v150
	v_fma_f32 v55, -v61, v151, v55
	v_lshlrev_b32_e32 v61, 16, v223
	v_mul_f32_e32 v152, 0xbfb8aa3b, v61
	v_exp_f32_e32 v152, v152
	v_div_fmas_f32 v55, v55, v150, v151
	v_div_fixup_f32 v55, v55, v57, v148
	v_mul_f32_e32 v51, v55, v51
	v_add_f32_e32 v57, 1.0, v152
	v_div_scale_f32 v148, s[34:35], v57, v57, v61
	v_rcp_f32_e32 v150, v148
	v_mul_f32_e32 v55, v161, v1
	v_mul_f32_e32 v52, v214, v55
	v_med3_f32 v51, v51, s83, v238
	v_fma_f32 v55, -v148, v150, 1.0
	v_fmac_f32_e32 v150, v55, v150
	v_div_scale_f32 v55, vcc, v61, v57, v61
	v_mul_f32_e32 v151, v55, v150
	v_fma_f32 v152, -v148, v151, v55
	v_fmac_f32_e32 v151, v152, v150
	v_fma_f32 v55, -v148, v151, v55
	v_and_b32_e32 v148, 0xffff0000, v223
	v_mul_f32_e32 v149, 0xbfb8aa3b, v148
	v_exp_f32_e32 v149, v149
	v_div_fmas_f32 v55, v55, v150, v151
	v_div_fixup_f32 v55, v55, v57, v61
	v_mul_f32_e32 v52, v55, v52
	v_add_f32_e32 v57, 1.0, v149
	v_div_scale_f32 v61, s[34:35], v57, v57, v148
	v_rcp_f32_e32 v149, v61
	v_mul_f32_e32 v55, v168, v1
	v_mul_f32_e32 v53, v215, v55
	v_fma_f32 v55, -v61, v149, 1.0
	v_fmac_f32_e32 v149, v55, v149
	v_div_scale_f32 v55, vcc, v148, v57, v148
	v_mul_f32_e32 v150, v55, v149
	v_fma_f32 v151, -v61, v150, v55
	v_fmac_f32_e32 v150, v151, v149
	v_fma_f32 v55, -v61, v150, v55
	v_div_fmas_f32 v55, v55, v149, v150
	v_div_fixup_f32 v55, v55, v57, v148
	v_mov_b32_e32 v57, v0
	v_cvt_pk_fp8_f32 v57, v50, v51
	v_mul_f32_e32 v50, v55, v53
	v_med3_f32 v51, v52, s83, v238
	v_med3_f32 v50, v50, s83, v238
	v_cvt_pk_fp8_f32 v57, v51, v50 op_sel:[0,0,1]
	v_mul_f32_e32 v55, v166, v1
	global_store_dword v[58:59], v57, off offset:16
	v_mul_f32_e32 v57, v165, v1
	v_lshlrev_b32_e32 v61, 16, v242
	v_mul_f32_e32 v150, 0xbfb8aa3b, v61
	v_and_b32_e32 v148, 0xffff0000, v242
	v_exp_f32_e32 v150, v150
	v_mul_f32_e32 v151, 0xbfb8aa3b, v148
	v_exp_f32_e32 v151, v151
	v_mul_f32_e32 v50, v216, v55
	v_add_f32_e32 v55, 1.0, v150
	v_div_scale_f32 v150, s[34:35], v55, v55, v61
	v_mul_f32_e32 v51, v217, v57
	v_add_f32_e32 v57, 1.0, v151
	v_rcp_f32_e32 v152, v150
	v_div_scale_f32 v151, s[34:35], v57, v57, v148
	v_rcp_f32_e32 v153, v151
	v_fma_f32 v155, -v150, v152, 1.0
	v_div_scale_f32 v154, vcc, v61, v55, v61
	v_fmac_f32_e32 v152, v155, v152
	v_fma_f32 v156, -v151, v153, 1.0
; __device__ __forceinline__ float silu_f(float x) { return x / (1.f + __expf(-x)); }
; __device__ __forceinline__ unsigned pk4_f8(float a, float b, float c, float d) {
;     a = fminf(fmaxf(a, -448.f), 448.f); b = fminf(fmaxf(b, -448.f), 448.f); c = fminf(fmaxf(c, -448.f), 448.f); d = fminf(fmaxf(d, -448.f), 448.f);
;     int r = 0; r = __builtin_amdgcn_cvt_pk_fp8_f32(a, b, r, false); r = __builtin_amdgcn_cvt_pk_fp8_f32(c, d, r, true); return (unsigned)r; }
; __device__ __forceinline__ void gla_pass_b(KP Pk, Frame& F, int l, int b, int h, int c, LAS unsigned char* wl) {
;     ...
;                 for (int nb = 0; nb < 4; ++nb) { const int dv0 = 16 * nb + 4 * kg; const u32x2 gg = *(const u32x2*)(U + (size_t)row * NU + UC_GG + h * 64 + dv0); const f32x4 nw = *(const f32x4*)(Pk->in[I_GNW] + l * 64 + dv0);
;                     const float y0 = o[nb][0] * rstd * nw[0] * silu_f(bflo(gg.x)), y1 = o[nb][1] * rstd * nw[1] * silu_f(bfhi(gg.x)), y2 = o[nb][2] * rstd * nw[2] * silu_f(bflo(gg.y)), y3 = o[nb][3] * rstd * nw[3] * silu_f(bfhi(gg.y));
;                     if (WOUT_F8) *(unsigned*)(MIX + ((size_t)row * D + h * 64 + dv0)) = pk4_f8(y0, y1, y2, y3);
	v_mul_f32_e32 v155, v154, v152
	v_fmac_f32_e32 v153, v156, v153
	v_fma_f32 v156, -v150, v155, v154
	v_fmac_f32_e32 v155, v156, v152
	v_fma_f32 v150, -v150, v155, v154
	v_div_fmas_f32 v150, v150, v152, v155
	v_div_fixup_f32 v55, v150, v55, v61
	v_mul_f32_e32 v50, v50, v55
	v_div_scale_f32 v55, vcc, v148, v57, v148
	v_mul_f32_e32 v61, v55, v153
	v_fma_f32 v150, -v151, v61, v55
	v_fmac_f32_e32 v61, v150, v153
	v_lshlrev_b32_e32 v150, 16, v243
	v_fma_f32 v55, -v151, v61, v55
	v_mul_f32_e32 v151, 0xbfb8aa3b, v150
	v_exp_f32_e32 v151, v151
	v_div_fmas_f32 v55, v55, v153, v61
	v_div_fixup_f32 v55, v55, v57, v148
	v_mul_f32_e32 v51, v51, v55
	v_add_f32_e32 v57, 1.0, v151
	v_div_scale_f32 v61, s[34:35], v57, v57, v150
	v_rcp_f32_e32 v148, v61
	v_mul_f32_e32 v55, v144, v1
	v_mul_f32_e32 v52, v218, v55
	v_med3_f32 v50, v50, s83, v238
	v_fma_f32 v55, -v61, v148, 1.0
	v_fmac_f32_e32 v148, v55, v148
	v_div_scale_f32 v55, vcc, v150, v57, v150
	v_mul_f32_e32 v144, v55, v148
	v_fma_f32 v151, -v61, v144, v55
	v_fmac_f32_e32 v144, v151, v148
	v_fma_f32 v55, -v61, v144, v55
	v_and_b32_e32 v61, 0xffff0000, v243
	v_mul_f32_e32 v149, 0xbfb8aa3b, v61
	v_exp_f32_e32 v149, v149
	v_div_fmas_f32 v55, v55, v148, v144
	v_div_fixup_f32 v55, v55, v57, v150
	v_mul_f32_e32 v52, v52, v55
	v_add_f32_e32 v57, 1.0, v149
	v_div_scale_f32 v144, s[34:35], v57, v57, v61
	v_rcp_f32_e32 v148, v144
	v_mul_f32_e32 v55, v145, v1
	v_mul_f32_e32 v53, v219, v55
	v_med3_f32 v51, v51, s83, v238
	v_fma_f32 v55, -v144, v148, 1.0
	v_fmac_f32_e32 v148, v55, v148
	v_div_scale_f32 v55, vcc, v61, v57, v61
	v_mul_f32_e32 v145, v55, v148
	v_fma_f32 v149, -v144, v145, v55
	v_fmac_f32_e32 v145, v149, v148
	v_fma_f32 v55, -v144, v145, v55
	v_div_fmas_f32 v55, v55, v148, v145
	v_div_fixup_f32 v55, v55, v57, v61
	v_mov_b32_e32 v57, v0
	v_cvt_pk_fp8_f32 v57, v50, v51
	v_mul_f32_e32 v50, v53, v55
	v_med3_f32 v51, v52, s83, v238
	v_med3_f32 v50, v50, s83, v238
	v_cvt_pk_fp8_f32 v57, v51, v50 op_sel:[0,0,1]
	v_mul_f32_e32 v55, v60, v1
	global_store_dword v[58:59], v57, off offset:32
	s_nop 0
	v_mul_f32_e32 v57, v160, v1
	v_mul_f32_e32 v1, v54, v1
	v_mul_f32_e32 v50, v55, v244
	v_lshlrev_b32_e32 v55, 16, v248
	v_mul_f32_e32 v51, v57, v245
	v_and_b32_e32 v57, 0xffff0000, v248
	v_lshlrev_b32_e32 v60, 16, v249
	v_mul_f32_e32 v61, 0xbfb8aa3b, v55
	v_mul_f32_e32 v142, 0xbfb8aa3b, v57
	v_mul_f32_e32 v144, 0xbfb8aa3b, v60
	v_exp_f32_e32 v61, v61
	v_exp_f32_e32 v142, v142
	v_exp_f32_e32 v144, v144
	v_mul_f32_e32 v52, v56, v246
	v_add_f32_e32 v56, 1.0, v61
	v_add_f32_e32 v61, 1.0, v142
	v_add_f32_e32 v142, 1.0, v144
	v_div_scale_f32 v144, s[34:35], v56, v56, v55
	v_div_scale_f32 v146, s[34:35], v61, v61, v57
	v_rcp_f32_e32 v148, v144
	v_rcp_f32_e32 v149, v146
	v_div_scale_f32 v145, vcc, v55, v56, v55
	v_fma_f32 v152, -v144, v148, 1.0
	v_fma_f32 v153, -v146, v149, 1.0
	v_fmac_f32_e32 v148, v152, v148
	v_div_scale_f32 v151, s[40:41], v57, v61, v57
	v_fmac_f32_e32 v149, v153, v149
	v_mul_f32_e32 v152, v145, v148
	v_div_scale_f32 v147, s[34:35], v142, v142, v60
	v_mul_f32_e32 v153, v151, v149
	v_fma_f32 v155, -v144, v152, v145
	v_rcp_f32_e32 v150, v147
	v_fma_f32 v156, -v146, v153, v151
	v_fmac_f32_e32 v152, v155, v148
	v_fmac_f32_e32 v153, v156, v149
	v_fma_f32 v144, -v144, v152, v145
	v_fma_f32 v145, -v146, v153, v151
	v_div_fmas_f32 v144, v144, v148, v152
	s_mov_b64 vcc, s[40:41]
	v_div_fixup_f32 v55, v144, v56, v55
	v_div_fmas_f32 v56, v145, v149, v153
	v_fma_f32 v154, -v147, v150, 1.0
	v_mul_f32_e32 v50, v50, v55
	v_div_fixup_f32 v55, v56, v61, v57
	v_mul_f32_e32 v51, v51, v55
	v_fmac_f32_e32 v150, v154, v150
	v_div_scale_f32 v55, vcc, v60, v142, v60
	v_mul_f32_e32 v56, v55, v150
	v_fma_f32 v57, -v147, v56, v55
	v_fmac_f32_e32 v56, v57, v150
	v_and_b32_e32 v57, 0xffff0000, v249
	v_mul_f32_e32 v61, 0xbfb8aa3b, v57
	v_exp_f32_e32 v61, v61
	v_fma_f32 v55, -v147, v56, v55
	v_div_fmas_f32 v55, v55, v150, v56
	v_div_fixup_f32 v55, v55, v142, v60
	v_add_f32_e32 v56, 1.0, v61
	v_div_scale_f32 v60, s[34:35], v56, v56, v57
	v_rcp_f32_e32 v61, v60
	v_mul_f32_e32 v1, v1, v247
	v_mul_f32_e32 v52, v52, v55
	v_med3_f32 v50, v50, s83, v238
	v_fma_f32 v53, -v60, v61, 1.0
	v_fmac_f32_e32 v61, v53, v61
	v_div_scale_f32 v53, vcc, v57, v56, v57
	v_mul_f32_e32 v54, v53, v61
	v_fma_f32 v55, -v60, v54, v53
	v_fmac_f32_e32 v54, v55, v61
	v_fma_f32 v53, -v60, v54, v53
	v_div_fmas_f32 v53, v53, v61, v54
	v_med3_f32 v51, v51, s83, v238
	v_mov_b32_e32 v54, v0
	v_cvt_pk_fp8_f32 v54, v50, v51
	v_div_fixup_f32 v53, v53, v56, v57
	v_mul_f32_e32 v1, v1, v53
	v_med3_f32 v50, v52, s83, v238
	v_med3_f32 v1, v1, s83, v238
	v_cvt_pk_fp8_f32 v54, v50, v1 op_sel:[0,0,1]
	global_store_dword v[58:59], v54, off offset:48
	s_branch .LBB0_660
